# all four scanner waves of a block share each row (a quarter each, own raw lists, 4 buffers), 250 rows streamed concurrently; gatherer fast path merges four lists
# speedup vs baseline: 1.0299x; 1.0154x over previous
_Z11attn_kernelPKfS0_PKDv8_DF16_S0_Pfi:
	s_load_dwordx2 s[28:29], s[0:1], 0x0
	v_cmp_gt_u32_e32 vcc, 16, v0
	s_and_saveexec_b64 s[4:5], vcc
	v_lshlrev_b32_e32 v1, 2, v0
	v_mov_b32_e32 v2, 0
	ds_write_b32 v1, v2 offset:36864
	s_or_b64 exec, exec, s[4:5]
	s_load_dword s33, s[0:1], 0x28
	v_bfe_u32 v1, v0, 6, 2
	v_lshl_or_b32 v82, s2, 2, v1
	v_readfirstlane_b32 s34, v0
	s_cmp_gt_u32 s34, 0xff
	s_cbranch_scc1 .Lsc_early_skip
	v_and_b32_e32 v3, 63, v0
	v_lshlrev_b32_e32 v2, 4, v3
	s_lshr_b32 s55, s34, 6
	s_mul_i32 s43, s55, 0x2800
	s_mov_b32 s37, s2
	s_and_b32 s47, s37, 1
	s_lshl_b32 s47, s47, 2
	s_mul_i32 s38, s37, 0x9c40
	s_lshl_b32 s40, s47, 4
	s_sub_u32 s38, s38, s40
	s_add_u32 s38, s38, s43
	s_waitcnt lgkmcnt(0)
	s_and_b32 s29, s29, 0xffff
	s_mov_b32 s30, 0x17d78400
	s_mov_b32 s31, 0x20000
	v_mov_b32_e32 v12, v2
	v_mov_b32_e32 v4, v2
	s_cmp_lg_u32 s55, 0
	s_cbranch_scc1 .Lsc_flpa
	v_max_u32_e32 v12, s47, v3
	v_lshlrev_b32_e32 v12, 4, v12
.Lsc_flpa:
	s_cmp_lg_u32 s55, 3
	s_cbranch_scc1 .Lsc_flpb
	s_add_i32 s41, s47, 3
	v_min_u32_e32 v4, s41, v3
	v_lshlrev_b32_e32 v4, 4, v4
.Lsc_flpb:
	buffer_load_dwordx4 v[100:103], v12, s[28:31], s38 offen nt
	s_add_u32 s40, s38, 0x400
	buffer_load_dwordx4 v[104:107], v2, s[28:31], s40 offen nt
	s_add_u32 s40, s38, 0x800
	buffer_load_dwordx4 v[108:111], v2, s[28:31], s40 offen nt
	s_add_u32 s40, s38, 0xc00
	buffer_load_dwordx4 v[112:115], v2, s[28:31], s40 offen nt
	s_add_u32 s40, s38, 0x1000
	buffer_load_dwordx4 v[116:119], v2, s[28:31], s40 offen nt
	s_add_u32 s40, s38, 0x1400
	buffer_load_dwordx4 v[120:123], v2, s[28:31], s40 offen nt
	s_add_u32 s40, s38, 0x1800
	buffer_load_dwordx4 v[124:127], v2, s[28:31], s40 offen nt
	s_add_u32 s40, s38, 0x1c00
	buffer_load_dwordx4 v[128:131], v2, s[28:31], s40 offen nt
	s_add_u32 s40, s38, 0x2000
	buffer_load_dwordx4 v[132:135], v2, s[28:31], s40 offen nt
	s_add_u32 s40, s38, 0x2400
	buffer_load_dwordx4 v[136:139], v4, s[28:31], s40 offen nt
.Lsc_early_skip:
	s_waitcnt lgkmcnt(0)
	s_barrier
	v_cmp_gt_i32_e32 vcc, s33, v82
	s_and_saveexec_b64 s[4:5], vcc
	s_cbranch_execz .LBB1_384
	s_abs_i32 s3, s33
	v_cvt_f32_u32_e32 v2, s3
	s_movk_i32 s4, 0xff
	v_sub_u32_e32 v3, 0x270f, v82
	v_cmp_lt_u32_e32 vcc, s4, v0
	v_rcp_iflag_f32_e32 v2, v2
	v_sub_u32_e32 v5, 0, v3
	s_sub_i32 s4, 0, s3
	v_xor_b32_e32 v4, s33, v3
	v_mul_f32_e32 v2, 0x4f7ffffe, v2
	v_cvt_u32_f32_e32 v2, v2
	v_max_i32_e32 v3, v3, v5
	v_ashrrev_i32_e32 v4, 31, v4
	v_mul_lo_u32 v5, s4, v2
	v_mul_hi_u32 v5, v2, v5
	v_add_u32_e32 v2, v2, v5
	v_mul_hi_u32 v2, v3, v2
	v_mul_lo_u32 v5, v2, s3
	v_sub_u32_e32 v3, v3, v5
	v_add_u32_e32 v5, 1, v2
	v_cmp_le_u32_e64 s[4:5], s3, v3
	v_and_b32_e32 v83, 63, v0
	s_nop 0
	v_cndmask_b32_e64 v2, v2, v5, s[4:5]
	v_subrev_u32_e32 v5, s3, v3
	v_cndmask_b32_e64 v3, v3, v5, s[4:5]
	v_add_u32_e32 v5, 1, v2
	v_cmp_le_u32_e64 s[4:5], s3, v3
	s_nop 1
	v_cndmask_b32_e64 v2, v2, v5, s[4:5]
	v_xor_b32_e32 v2, v2, v4
	v_sub_u32_e32 v84, v2, v4
	s_and_saveexec_b64 s[4:5], vcc
	s_xor_b64 s[30:31], exec, s[4:5]
	s_cbranch_execz .LBB1_217
	v_cmp_lt_i32_e32 vcc, -1, v84
	s_and_saveexec_b64 s[34:35], vcc
	s_cbranch_execz .LBB1_216
	s_load_dwordx8 s[20:27], s[0:1], 0x8
	v_and_b32_e32 v69, 15, v0
	v_mov_b32_e32 v0, 0x8000
	v_lshrrev_b32_e32 v67, 4, v83
	v_lshl_or_b32 v88, v1, 10, v0
	s_mul_i32 s3, s2, 0x2710
	v_mul_u32_u24_e32 v0, 0x9c4, v1
	v_lshl_or_b32 v89, v69, 2, v67
	v_add3_u32 v90, s3, v0, v83
	v_lshlrev_b32_e32 v0, 2, v1
	v_mov_b32_e32 v2, 0x9000
	v_lshl_or_b32 v91, s2, 4, v0
	v_lshlrev_b32_e32 v0, 3, v89
	v_mov_b32_e32 v32, 0
	v_lshl_or_b32 v65, v1, 3, v2
	v_or_b32_e32 v2, 0x1e00, v0
	v_mov_b32_e32 v3, v32
	s_waitcnt lgkmcnt(0)
	v_lshl_add_u64 v[34:35], s[20:21], 0, v[2:3]
	v_or_b32_e32 v2, 0x1c00, v0
	v_lshl_add_u64 v[36:37], s[20:21], 0, v[2:3]
	v_or_b32_e32 v2, 0x1a00, v0
	v_lshl_add_u64 v[38:39], s[20:21], 0, v[2:3]
	v_or_b32_e32 v2, 0x1800, v0
	v_lshl_add_u64 v[40:41], s[20:21], 0, v[2:3]
	v_or_b32_e32 v2, 0x1600, v0
	v_lshl_add_u64 v[42:43], s[20:21], 0, v[2:3]
	v_or_b32_e32 v2, 0x1400, v0
	v_lshlrev_b32_e32 v63, 12, v1
	v_lshl_add_u64 v[44:45], s[20:21], 0, v[2:3]
	v_or_b32_e32 v2, 0x1200, v0
	v_mov_b32_e32 v1, v32
	v_lshl_or_b32 v71, v83, 3, v63
	v_lshl_or_b32 v73, v67, 3, v63
	v_lshl_add_u64 v[46:47], s[20:21], 0, v[2:3]
	v_or_b32_e32 v2, 0x1000, v0
	v_lshl_add_u64 v[50:51], s[20:21], 0, v[0:1]
	v_mbcnt_lo_u32_b32 v0, -1, 0
	v_or_b32_e32 v75, 4, v67
	v_or_b32_e32 v77, 8, v67
	v_or_b32_e32 v78, 12, v67
	v_or_b32_e32 v79, 16, v67
	v_or_b32_e32 v80, 20, v67
	v_or_b32_e32 v81, 24, v67
	v_or_b32_e32 v85, 28, v67
	v_or_b32_e32 v86, 64, v83
	v_or_b32_e32 v87, 0x4000, v63
	v_cmp_lt_u32_e64 s[0:1], 15, v83
	s_mul_i32 s39, s33, 0x9c4
	s_lshl_b32 s48, s33, 2
	v_or_b32_e32 v92, 0x200, v71
	v_or_b32_e32 v93, 0x204, v71
	v_or_b32_e32 v94, 0x100, v73
	v_lshl_add_u64 v[48:49], s[20:21], 0, v[2:3]
	s_mov_b32 s51, 0
	s_mov_b64 s[36:37], 0
	s_movk_i32 s49, 0x81
	s_mov_b32 s50, 0xff800000
	s_mov_b32 s38, 0x38d1b717
	v_mov_b32_e32 v95, 0xff800000
	v_mbcnt_hi_u32_b32 v96, -1, v0
	v_mov_b32_e32 v136, 0
	v_mov_b32_e32 v137, 0
	v_mov_b32_e32 v138, 0
	v_mov_b32_e32 v139, 0
	v_mov_b32_e32 v140, 0
	v_mov_b32_e32 v141, 0
	v_mov_b32_e32 v142, 0
	v_mov_b32_e32 v143, 0
	v_mov_b32_e32 v144, 0
	v_mov_b32_e32 v145, 0
	v_mov_b32_e32 v146, 0
	v_mov_b32_e32 v147, 0
	v_mov_b32_e32 v148, 0
	v_mov_b32_e32 v149, 0
	v_mov_b32_e32 v150, 0
	v_mov_b32_e32 v151, 0
	v_mov_b32_e32 v152, 0
	v_mov_b32_e32 v153, 0
	v_mov_b32_e32 v154, 0
	v_mov_b32_e32 v155, 0
	v_mov_b32_e32 v156, 0
	v_mov_b32_e32 v157, 0
	v_mov_b32_e32 v158, 0
	v_mov_b32_e32 v159, 0
	v_mov_b32_e32 v160, 0
	v_mov_b32_e32 v161, 0
	v_mov_b32_e32 v162, 0
	v_mov_b32_e32 v163, 0
	v_mov_b32_e32 v164, 0
	v_mov_b32_e32 v165, 0
	v_mov_b32_e32 v166, 0
	v_mov_b32_e32 v167, 0
	v_mov_b32_e32 v168, 0
	v_mov_b32_e32 v169, 0
	v_mov_b32_e32 v170, 0
	v_mov_b32_e32 v171, 0
	v_mov_b32_e32 v172, 0
	v_mov_b32_e32 v173, 0
	v_mov_b32_e32 v174, 0
	v_mov_b32_e32 v175, 0
	v_mov_b32_e32 v176, 0
	v_mov_b32_e32 v177, 0
	v_mov_b32_e32 v178, 0
	v_mov_b32_e32 v179, 0
	v_mov_b32_e32 v180, 0
	v_mov_b32_e32 v181, 0
	v_mov_b32_e32 v182, 0
	v_mov_b32_e32 v183, 0
	v_mov_b32_e32 v184, 0
	v_mov_b32_e32 v185, 0
	v_mov_b32_e32 v186, 0
	v_mov_b32_e32 v187, 0
	v_mov_b32_e32 v188, 0
	v_mov_b32_e32 v189, 0
	v_mov_b32_e32 v190, 0
	v_mov_b32_e32 v191, 0
	v_mov_b32_e32 v192, 0
	v_mov_b32_e32 v193, 0
	v_mov_b32_e32 v194, 0
	v_mov_b32_e32 v195, 0
	v_mov_b32_e32 v196, 0
	v_mov_b32_e32 v197, 0
	v_mov_b32_e32 v198, 0
	v_mov_b32_e32 v199, 0
	v_readfirstlane_b32 s54, v63
	s_lshr_b32 s54, s54, 12
	s_mul_i32 s4, s54, 0xfa
	s_add_u32 s4, s4, s2
	v_mov_b32_e32 v82, s4
	v_mov_b32_e32 v87, 0x4000
	v_mov_b32_e32 v88, 0x8000
	v_mov_b32_e32 v65, 0x9030
	s_movk_i32 s3, 0x9c4
	v_mad_u32_u24 v90, v82, s3, v83
	v_lshlrev_b32_e32 v91, 2, v82
	s_branch .LBB1_9

.LBB1_13:
	s_or_b64 exec, exec, s[2:3]
	s_mul_i32 s2, s51, s33
	v_add_u32_e32 v97, s2, v82
	v_readfirstlane_b32 s5, v0
	s_sub_i32 s5, s5, 1
	v_add_u32_e32 v7, -48, v6
	s_mov_b32 s19, 0x40000
.Lg_poll0:
	ds_read_b32 v1, v7
	s_waitcnt lgkmcnt(0)
	v_readfirstlane_b32 s4, v1
	s_cmp_lg_u32 s4, 0
	s_cbranch_scc1 .Lg_got0
	s_sub_u32 s19, s19, 1
	s_cmp_eq_u32 s19, 0
	s_cbranch_scc1 .Lg_got0
	s_sleep 1
	s_branch .Lg_poll0
.Lg_got0:
	s_mov_b32 s19, 0x40000
.Lg_poll1:
	ds_read_b32 v1, v7 offset:16
	s_waitcnt lgkmcnt(0)
	v_readfirstlane_b32 s16, v1
	s_cmp_lg_u32 s16, 0
	s_cbranch_scc1 .Lg_got1
	s_sub_u32 s19, s19, 1
	s_cmp_eq_u32 s19, 0
	s_cbranch_scc1 .Lg_got1
	s_sleep 1
	s_branch .Lg_poll1

.Lg_poll2:
	ds_read_b32 v1, v7 offset:32
	s_waitcnt lgkmcnt(0)
	v_readfirstlane_b32 s17, v1
	s_cmp_lg_u32 s17, 0
	s_cbranch_scc1 .Lg_got2
	s_sub_u32 s19, s19, 1
	s_cmp_eq_u32 s19, 0
	s_cbranch_scc1 .Lg_got2
	s_sleep 1
	s_branch .Lg_poll2
.Lg_got2:
	s_sub_i32 s4, s4, 1
	s_cmp_gt_u32 s4, 64
	s_cbranch_scc1 .Lg_fb
	s_sub_i32 s16, s16, 1
	s_cmp_gt_u32 s16, 64
	s_cbranch_scc1 .Lg_fb
	s_sub_i32 s17, s17, 1
	s_cmp_gt_u32 s17, 64
	s_cbranch_scc1 .Lg_fb
	s_cmp_gt_u32 s5, 64
	s_cbranch_scc1 .Lg_fb
	s_add_i32 s16, s16, s4
	s_add_i32 s17, s17, s16
	s_add_i32 s18, s17, s5
	s_cmp_gt_u32 s18, 64
	s_cbranch_scc1 .Lg_fb
	v_cmp_gt_u32_e64 s[8:9], s4, v83
	v_cmp_gt_u32_e64 s[10:11], s16, v83
	v_cmp_gt_u32_e64 s[12:13], s17, v83
	v_subrev_u32_e32 v1, s4, v83
	v_add_u32_e32 v1, 0x100, v1
	v_subrev_u32_e32 v2, s16, v83
	v_add_u32_e32 v2, 0x200, v2
	v_subrev_u32_e32 v13, s17, v83
	v_add_u32_e32 v13, 0x300, v13
	v_cndmask_b32_e64 v13, v13, v2, s[12:13]
	v_cndmask_b32_e64 v13, v13, v1, s[10:11]
	v_cndmask_b32_e64 v13, v13, v83, s[8:9]
	s_lshl_b32 s19, s46, 10
	v_lshl_add_u32 v1, v13, 4, v87
	v_add_u32_e32 v1, s19, v1
	s_lshl_b32 s19, s46, 8
	v_lshl_add_u32 v2, v13, 2, v88
	v_add_u32_e32 v2, s19, v2
	ds_read_b128 v[8:11], v1
	ds_read_b32 v12, v2
	v_cmp_gt_u32_e64 s[6:7], s18, v83
	v_lshlrev_b32_e32 v25, 4, v69
	s_waitcnt lgkmcnt(0)
	v_cmp_neq_f32_e32 vcc, 0, v8
	s_and_b64 s[8:9], vcc, s[6:7]
	v_cmp_neq_f32_e32 vcc, 0, v9
	s_and_b64 s[10:11], vcc, s[6:7]
	v_cmp_neq_f32_e32 vcc, 0, v10
	s_and_b64 s[12:13], vcc, s[6:7]
	v_cmp_neq_f32_e32 vcc, 0, v11
	s_and_b64 s[14:15], vcc, s[6:7]
	s_bcnt1_i32_b64 s16, s[8:9]
	s_bcnt1_i32_b64 s17, s[10:11]
	s_bcnt1_i32_b64 s18, s[12:13]
	s_bcnt1_i32_b64 s19, s[14:15]
	s_add_i32 s17, s17, s16
	s_add_i32 s18, s18, s17
	s_add_i32 s19, s19, s18
	s_cmp_eq_u32 s19, 0
	s_cbranch_scc1 .Lg_fb
	s_cmp_gt_u32 s19, 64
	s_cbranch_scc1 .Lg_fb
	v_mbcnt_lo_u32_b32 v13, s8, 0
	v_mbcnt_hi_u32_b32 v13, s9, v13
	v_lshl_add_u32 v14, v13, 3, v63
	v_mov_b32_e32 v4, v12
	v_mov_b32_e32 v5, v8
	s_mov_b64 exec, s[8:9]
	ds_write_b64 v14, v[4:5]
	s_mov_b64 exec, -1
	v_mbcnt_lo_u32_b32 v13, s10, 0
	v_mbcnt_hi_u32_b32 v13, s11, v13
	v_add_u32_e32 v13, s16, v13
	v_lshl_add_u32 v14, v13, 3, v63
	v_add_u32_e32 v4, 1, v12
	v_mov_b32_e32 v5, v9
	s_mov_b64 exec, s[10:11]
	ds_write_b64 v14, v[4:5]
	s_mov_b64 exec, -1
	v_mbcnt_lo_u32_b32 v13, s12, 0
	v_mbcnt_hi_u32_b32 v13, s13, v13
	v_add_u32_e32 v13, s17, v13
	v_lshl_add_u32 v14, v13, 3, v63
	v_add_u32_e32 v4, 2, v12
	v_mov_b32_e32 v5, v10
	s_mov_b64 exec, s[12:13]
	ds_write_b64 v14, v[4:5]
	s_mov_b64 exec, -1
	v_mbcnt_lo_u32_b32 v13, s14, 0
	v_mbcnt_hi_u32_b32 v13, s15, v13
	v_add_u32_e32 v13, s18, v13
	v_lshl_add_u32 v14, v13, 3, v63
	v_add_u32_e32 v4, 3, v12
	v_mov_b32_e32 v5, v11
	s_mov_b64 exec, s[14:15]
	ds_write_b64 v14, v[4:5]
	s_mov_b64 exec, -1
	v_mov_b32_e32 v4, 0
	ds_write_b32 v6, v4
	ds_write_b32 v7, v4
	ds_write_b32 v7, v4 offset:16
	ds_write_b32 v7, v4 offset:32
	v_cmp_gt_u32_e64 s[6:7], s19, v83
	v_lshl_add_u32 v14, v83, 3, v63
	ds_read_b64 v[16:17], v14
	v_lshl_add_u32 v22, v67, 3, v63
	ds_read_b32 v116, v22
	ds_read_b32 v117, v22 offset:32
	ds_read_b32 v118, v22 offset:64
	ds_read_b32 v119, v22 offset:96
	ds_read_b32 v120, v22 offset:128
	ds_read_b32 v121, v22 offset:160
	ds_read_b32 v122, v22 offset:192
	ds_read_b32 v123, v22 offset:224
	v_sub_u32_e32 v23, s19, v67
	s_waitcnt lgkmcnt(8)
	v_cndmask_b32_e64 v15, 0, v16, s[6:7]
	v_lshlrev_b32_e32 v15, 2, v15
	global_load_dword v18, v15, s[24:25]
	s_cmp_gt_u32 s19, 32
	s_cbranch_scc1 .Lg_big
	s_waitcnt lgkmcnt(0)
	v_cmp_lt_i32_e32 vcc, 0, v23
	v_lshl_add_u32 v24, v116, 8, v25
	s_mov_b64 exec, vcc
	global_load_dwordx4 v[136:139], v24, s[22:23]
	s_mov_b64 exec, -1
	v_cmp_lt_i32_e32 vcc, 4, v23
	v_lshl_add_u32 v24, v117, 8, v25
	s_mov_b64 exec, vcc
	global_load_dwordx4 v[140:143], v24, s[22:23]
	s_mov_b64 exec, -1
	v_cmp_lt_i32_e32 vcc, 8, v23
	v_lshl_add_u32 v24, v118, 8, v25
	s_mov_b64 exec, vcc
	global_load_dwordx4 v[144:147], v24, s[22:23]
	s_mov_b64 exec, -1
	v_cmp_lt_i32_e32 vcc, 12, v23
	v_lshl_add_u32 v24, v119, 8, v25
	s_mov_b64 exec, vcc
	global_load_dwordx4 v[148:151], v24, s[22:23]
	s_mov_b64 exec, -1
	v_cmp_lt_i32_e32 vcc, 16, v23
	v_lshl_add_u32 v24, v120, 8, v25
	s_mov_b64 exec, vcc
	global_load_dwordx4 v[152:155], v24, s[22:23]
	s_mov_b64 exec, -1
	v_cmp_lt_i32_e32 vcc, 20, v23
	v_lshl_add_u32 v24, v121, 8, v25
	s_mov_b64 exec, vcc
	global_load_dwordx4 v[156:159], v24, s[22:23]
	s_mov_b64 exec, -1
	v_cmp_lt_i32_e32 vcc, 24, v23
	v_lshl_add_u32 v24, v122, 8, v25
	s_mov_b64 exec, vcc
	global_load_dwordx4 v[160:163], v24, s[22:23]
	s_mov_b64 exec, -1
	v_cmp_lt_i32_e32 vcc, 28, v23
	v_lshl_add_u32 v24, v123, 8, v25
	s_mov_b64 exec, vcc
	global_load_dwordx4 v[164:167], v24, s[22:23]
	s_mov_b64 exec, -1
	s_waitcnt vmcnt(8)
	s_branch .Lg_soft

.Lg_fb:
	v_mov_b32_e32 v4, 0
	ds_write_b32 v7, v4
	ds_write_b32 v7, v4 offset:16
	ds_write_b32 v7, v4 offset:32
	v_mov_b32_e32 v0, 0xc8

.LBB1_217:
	s_andn2_saveexec_b64 s[0:1], s[30:31]
	s_cbranch_execz .LBB1_384
	v_readfirstlane_b32 s34, v1
	v_readfirstlane_b32 s36, v84
	v_and_b32_e32 v3, 63, v0
	v_lshlrev_b32_e32 v2, 4, v3
	s_cmp_lt_i32 s36, 0
	s_cbranch_scc1 .LBB1_384
	s_add_i32 s36, s36, 1
	s_lshl_b32 s36, s36, 2
	s_sub_i32 s36, s36, 1
	s_lshr_b32 s33, s33, 2
	s_mov_b32 s55, s34
	s_mul_i32 s43, s55, 0x2800
	s_mov_b32 s37, s2
	s_waitcnt lgkmcnt(0)
	s_and_b32 s29, s29, 0xffff
	s_mov_b32 s30, 0x17d78400
	s_mov_b32 s31, 0x20000
	s_mov_b32 s35, 0
	s_movk_i32 s7, 0x40
	s_mov_b32 s9, 0x7fffffff
	s_lshl_b32 s44, s34, 12
	s_add_u32 s44, s44, 0x4000
	s_lshl_b32 s45, s34, 10
	s_add_u32 s45, s45, 0x8000
	s_lshl_b32 s46, s34, 4
	s_add_u32 s46, s46, 0x9000
	s_and_b32 s47, s37, 1
	s_lshl_b32 s47, s47, 2
	s_mul_i32 s38, s37, 0x9c40
	s_lshl_b32 s40, s47, 4
	s_sub_u32 s38, s38, s40
	s_add_u32 s38, s38, s43
.Lsc_row:
	v_subrev_u32_e32 v8, s47, v3
	v_lshlrev_b32_e32 v8, 2, v8
	s_mul_i32 s40, s55, 0xa00
	v_add_u32_e32 v8, s40, v8
	s_mov_b64 s[48:49], -1
	s_mov_b64 s[50:51], -1
	s_cmp_lg_u32 s55, 0
	s_cbranch_scc1 .Lsc_m0
	s_lshl_b64 s[48:49], -1, s47
.Lsc_m0:
	s_cmp_lg_u32 s55, 3
	s_cbranch_scc1 .Lsc_m3
	s_add_i32 s41, s47, 3
	s_lshl_b64 s[50:51], 2, s41
	s_sub_u32 s50, s50, 1
	s_subb_u32 s51, s51, 0
.Lsc_m3:
	s_and_b32 s41, s35, 3
	s_lshl_b32 s40, s41, 10
	s_add_u32 s40, s40, s44
	v_mov_b32_e32 v9, s40
	s_lshl_b32 s40, s41, 8
	s_add_u32 s40, s40, s45
	v_mov_b32_e32 v10, s40
	s_lshl_b32 s40, s41, 2
	s_add_u32 s40, s40, s46
	v_mov_b32_e32 v11, s40
	s_cmp_lt_i32 s35, s36
	s_cbranch_scc0 .Lsc_nonext
	s_add_i32 s52, s37, s33
	s_and_b32 s53, s52, 1
	s_lshl_b32 s53, s53, 2
	s_mul_i32 s39, s52, 0x9c40
	s_lshl_b32 s40, s53, 4
	s_sub_u32 s39, s39, s40
	s_add_u32 s39, s39, s43
	v_mov_b32_e32 v6, v2
	v_mov_b32_e32 v5, v2
	v_mov_b32_e32 v7, v2
	s_cmp_lg_u32 s55, 0
	s_cbranch_scc1 .Lsc_n0
	v_max_u32_e32 v5, s53, v3
	v_lshlrev_b32_e32 v5, 4, v5
.Lsc_n0:
	s_cmp_lg_u32 s55, 3
	s_cbranch_scc1 .Lsc_gotnext
	s_add_i32 s40, s53, 3
	v_min_u32_e32 v7, s40, v3
	v_lshlrev_b32_e32 v7, 4, v7
	s_branch .Lsc_gotnext

.Lsc_s0:
	s_mov_b32 s40, s39
	buffer_load_dwordx4 v[100:103], v5, s[28:31], s40 offen nt
	s_waitcnt vmcnt(9)
	v_or3_b32 v12, v104, v105, v106
	v_bitop3_b32 v12, v12, s9, v107 bitop3:0xc8
	v_cmp_ne_u32_e32 vcc, 0, v12
	s_cbranch_vccz .Lsc_s1
	s_bcnt1_i32_b64 s40, vcc
	v_mbcnt_lo_u32_b32 v13, vcc_lo, 0
	v_mbcnt_hi_u32_b32 v13, vcc_hi, v13
	v_add_u32_e32 v13, s42, v13
	s_add_i32 s42, s42, s40
	v_cmp_gt_i32_e64 s[0:1], s7, v13
	s_and_b64 s[4:5], vcc, s[0:1]
	s_and_saveexec_b64 s[0:1], s[4:5]
	v_lshl_add_u32 v14, v13, 4, v9
	v_lshl_add_u32 v15, v13, 2, v10
	v_add_u32_e32 v13, 0x100, v8
	ds_write_b128 v14, v[104:107]
	ds_write_b32 v15, v13
	s_mov_b64 exec, -1
.Lsc_s1:
	s_add_u32 s40, s39, 0x400
	buffer_load_dwordx4 v[104:107], v6, s[28:31], s40 offen nt
	s_waitcnt vmcnt(9)
	v_or3_b32 v12, v108, v109, v110
	v_bitop3_b32 v12, v12, s9, v111 bitop3:0xc8
	v_cmp_ne_u32_e32 vcc, 0, v12
	s_cbranch_vccz .Lsc_s2
	s_bcnt1_i32_b64 s40, vcc
	v_mbcnt_lo_u32_b32 v13, vcc_lo, 0
	v_mbcnt_hi_u32_b32 v13, vcc_hi, v13
	v_add_u32_e32 v13, s42, v13
	s_add_i32 s42, s42, s40
	v_cmp_gt_i32_e64 s[0:1], s7, v13
	s_and_b64 s[4:5], vcc, s[0:1]
	s_and_saveexec_b64 s[0:1], s[4:5]
	v_lshl_add_u32 v14, v13, 4, v9
	v_lshl_add_u32 v15, v13, 2, v10
	v_add_u32_e32 v13, 0x200, v8
	ds_write_b128 v14, v[108:111]
	ds_write_b32 v15, v13
	s_mov_b64 exec, -1
.Lsc_s2:
	s_add_u32 s40, s39, 0x800
	buffer_load_dwordx4 v[108:111], v6, s[28:31], s40 offen nt
	s_waitcnt vmcnt(9)
	v_or3_b32 v12, v112, v113, v114
	v_bitop3_b32 v12, v12, s9, v115 bitop3:0xc8
	v_cmp_ne_u32_e32 vcc, 0, v12
	s_cbranch_vccz .Lsc_s3
	s_bcnt1_i32_b64 s40, vcc
	v_mbcnt_lo_u32_b32 v13, vcc_lo, 0
	v_mbcnt_hi_u32_b32 v13, vcc_hi, v13
	v_add_u32_e32 v13, s42, v13
	s_add_i32 s42, s42, s40
	v_cmp_gt_i32_e64 s[0:1], s7, v13
	s_and_b64 s[4:5], vcc, s[0:1]
	s_and_saveexec_b64 s[0:1], s[4:5]
	v_lshl_add_u32 v14, v13, 4, v9
	v_lshl_add_u32 v15, v13, 2, v10
	v_add_u32_e32 v13, 0x300, v8
	ds_write_b128 v14, v[112:115]
	ds_write_b32 v15, v13
	s_mov_b64 exec, -1
.Lsc_s3:
	s_add_u32 s40, s39, 0xc00
	buffer_load_dwordx4 v[112:115], v6, s[28:31], s40 offen nt
	s_waitcnt vmcnt(9)
	v_or3_b32 v12, v116, v117, v118
	v_bitop3_b32 v12, v12, s9, v119 bitop3:0xc8
	v_cmp_ne_u32_e32 vcc, 0, v12
	s_cbranch_vccz .Lsc_s4
	s_bcnt1_i32_b64 s40, vcc
	v_mbcnt_lo_u32_b32 v13, vcc_lo, 0
	v_mbcnt_hi_u32_b32 v13, vcc_hi, v13
	v_add_u32_e32 v13, s42, v13
	s_add_i32 s42, s42, s40
	v_cmp_gt_i32_e64 s[0:1], s7, v13
	s_and_b64 s[4:5], vcc, s[0:1]
	s_and_saveexec_b64 s[0:1], s[4:5]
	v_lshl_add_u32 v14, v13, 4, v9
	v_lshl_add_u32 v15, v13, 2, v10
	v_add_u32_e32 v13, 0x400, v8
	ds_write_b128 v14, v[116:119]
	ds_write_b32 v15, v13
	s_mov_b64 exec, -1
.Lsc_s4:
	s_add_u32 s40, s39, 0x1000
	buffer_load_dwordx4 v[116:119], v6, s[28:31], s40 offen nt
	s_waitcnt vmcnt(9)
	v_or3_b32 v12, v120, v121, v122
	v_bitop3_b32 v12, v12, s9, v123 bitop3:0xc8
	v_cmp_ne_u32_e32 vcc, 0, v12
	s_cbranch_vccz .Lsc_s5
	s_bcnt1_i32_b64 s40, vcc
	v_mbcnt_lo_u32_b32 v13, vcc_lo, 0
	v_mbcnt_hi_u32_b32 v13, vcc_hi, v13
	v_add_u32_e32 v13, s42, v13
	s_add_i32 s42, s42, s40
	v_cmp_gt_i32_e64 s[0:1], s7, v13
	s_and_b64 s[4:5], vcc, s[0:1]
	s_and_saveexec_b64 s[0:1], s[4:5]
	v_lshl_add_u32 v14, v13, 4, v9
	v_lshl_add_u32 v15, v13, 2, v10
	v_add_u32_e32 v13, 0x500, v8
	ds_write_b128 v14, v[120:123]
	ds_write_b32 v15, v13
	s_mov_b64 exec, -1
.Lsc_s5:
	s_add_u32 s40, s39, 0x1400
	buffer_load_dwordx4 v[120:123], v6, s[28:31], s40 offen nt
	s_waitcnt vmcnt(9)
	v_or3_b32 v12, v124, v125, v126
	v_bitop3_b32 v12, v12, s9, v127 bitop3:0xc8
	v_cmp_ne_u32_e32 vcc, 0, v12
	s_cbranch_vccz .Lsc_s6
	s_bcnt1_i32_b64 s40, vcc
	v_mbcnt_lo_u32_b32 v13, vcc_lo, 0
	v_mbcnt_hi_u32_b32 v13, vcc_hi, v13
	v_add_u32_e32 v13, s42, v13
	s_add_i32 s42, s42, s40
	v_cmp_gt_i32_e64 s[0:1], s7, v13
	s_and_b64 s[4:5], vcc, s[0:1]
	s_and_saveexec_b64 s[0:1], s[4:5]
	v_lshl_add_u32 v14, v13, 4, v9
	v_lshl_add_u32 v15, v13, 2, v10
	v_add_u32_e32 v13, 0x600, v8
	ds_write_b128 v14, v[124:127]
	ds_write_b32 v15, v13
	s_mov_b64 exec, -1
.Lsc_s6:
	s_add_u32 s40, s39, 0x1800
	buffer_load_dwordx4 v[124:127], v6, s[28:31], s40 offen nt
	s_waitcnt vmcnt(9)
	v_or3_b32 v12, v128, v129, v130
	v_bitop3_b32 v12, v12, s9, v131 bitop3:0xc8
	v_cmp_ne_u32_e32 vcc, 0, v12
	s_cbranch_vccz .Lsc_s7
	s_bcnt1_i32_b64 s40, vcc
	v_mbcnt_lo_u32_b32 v13, vcc_lo, 0
	v_mbcnt_hi_u32_b32 v13, vcc_hi, v13
	v_add_u32_e32 v13, s42, v13
	s_add_i32 s42, s42, s40
	v_cmp_gt_i32_e64 s[0:1], s7, v13
	s_and_b64 s[4:5], vcc, s[0:1]
	s_and_saveexec_b64 s[0:1], s[4:5]
	v_lshl_add_u32 v14, v13, 4, v9
	v_lshl_add_u32 v15, v13, 2, v10
	v_add_u32_e32 v13, 0x700, v8
	ds_write_b128 v14, v[128:131]
	ds_write_b32 v15, v13
	s_mov_b64 exec, -1
.Lsc_s7:
	s_add_u32 s40, s39, 0x1c00
	buffer_load_dwordx4 v[128:131], v6, s[28:31], s40 offen nt
	s_waitcnt vmcnt(9)
	v_or3_b32 v12, v132, v133, v134
	v_bitop3_b32 v12, v12, s9, v135 bitop3:0xc8
	v_cmp_ne_u32_e32 vcc, 0, v12
	s_cbranch_vccz .Lsc_s8
	s_bcnt1_i32_b64 s40, vcc
	v_mbcnt_lo_u32_b32 v13, vcc_lo, 0
	v_mbcnt_hi_u32_b32 v13, vcc_hi, v13
	v_add_u32_e32 v13, s42, v13
	s_add_i32 s42, s42, s40
	v_cmp_gt_i32_e64 s[0:1], s7, v13
	s_and_b64 s[4:5], vcc, s[0:1]
	s_and_saveexec_b64 s[0:1], s[4:5]
	v_lshl_add_u32 v14, v13, 4, v9
	v_lshl_add_u32 v15, v13, 2, v10
	v_add_u32_e32 v13, 0x800, v8
	ds_write_b128 v14, v[132:135]
	ds_write_b32 v15, v13
	s_mov_b64 exec, -1
.Lsc_s8:
	s_add_u32 s40, s39, 0x2000
	buffer_load_dwordx4 v[132:135], v6, s[28:31], s40 offen nt
	s_waitcnt vmcnt(9)
	v_or3_b32 v12, v136, v137, v138
	v_bitop3_b32 v12, v12, s9, v139 bitop3:0xc8
	v_cmp_ne_u32_e32 vcc, 0, v12
	s_and_b64 vcc, vcc, s[50:51]
	s_cbranch_vccz .Lsc_s9
	s_bcnt1_i32_b64 s40, vcc
	v_mbcnt_lo_u32_b32 v13, vcc_lo, 0
	v_mbcnt_hi_u32_b32 v13, vcc_hi, v13
	v_add_u32_e32 v13, s42, v13
	s_add_i32 s42, s42, s40
	v_cmp_gt_i32_e64 s[0:1], s7, v13
	s_and_b64 s[4:5], vcc, s[0:1]
	s_and_saveexec_b64 s[0:1], s[4:5]
	v_lshl_add_u32 v14, v13, 4, v9
	v_lshl_add_u32 v15, v13, 2, v10
	v_add_u32_e32 v13, 0x900, v8
	ds_write_b128 v14, v[136:139]
	ds_write_b32 v15, v13
	s_mov_b64 exec, -1
.Lsc_s9:
	s_add_u32 s40, s39, 0x2400
	buffer_load_dwordx4 v[136:139], v7, s[28:31], s40 offen nt
	s_waitcnt lgkmcnt(0)
	s_add_i32 s42, s42, 1
	v_mov_b32_e32 v12, s42
	ds_write_b32 v11, v12
	s_cmp_eq_u32 s35, s36
	s_cbranch_scc1 .LBB1_384
	s_add_i32 s35, s35, 1
	s_mov_b32 s37, s52
	s_mov_b32 s38, s39
	s_mov_b32 s47, s53
	s_branch .Lsc_row

	.amdhsa_kernel _Z11attn_kernelPKfS0_PKDv8_DF16_S0_Pfi
		.amdhsa_group_segment_fixed_size 36928
		.amdhsa_private_segment_fixed_size 0
		.amdhsa_kernarg_size 44
		.amdhsa_user_sgpr_count 2
		.amdhsa_user_sgpr_dispatch_ptr 0
		.amdhsa_user_sgpr_queue_ptr 0
		.amdhsa_user_sgpr_kernarg_segment_ptr 1
		.amdhsa_user_sgpr_dispatch_id 0
		.amdhsa_user_sgpr_kernarg_preload_length 0
		.amdhsa_user_sgpr_kernarg_preload_offset 0
		.amdhsa_user_sgpr_private_segment_size 0
		.amdhsa_uses_dynamic_stack 0
		.amdhsa_enable_private_segment 0
		.amdhsa_system_sgpr_workgroup_id_x 1
		.amdhsa_system_sgpr_workgroup_id_y 0
		.amdhsa_system_sgpr_workgroup_id_z 0
		.amdhsa_system_sgpr_workgroup_info 0
		.amdhsa_system_vgpr_workitem_id 0
		.amdhsa_next_free_vgpr 248
		.amdhsa_next_free_sgpr 58
		.amdhsa_accum_offset 248
		.amdhsa_reserve_vcc 1
		.amdhsa_float_round_mode_32 0
		.amdhsa_float_round_mode_16_64 0
		.amdhsa_float_denorm_mode_32 3
		.amdhsa_float_denorm_mode_16_64 3
		.amdhsa_dx10_clamp 1
		.amdhsa_ieee_mode 1
		.amdhsa_fp16_overflow 0
		.amdhsa_tg_split 0
		.amdhsa_exception_fp_ieee_invalid_op 0
		.amdhsa_exception_fp_denorm_src 0
		.amdhsa_exception_fp_ieee_div_zero 0
		.amdhsa_exception_fp_ieee_overflow 0
		.amdhsa_exception_fp_ieee_underflow 0
		.amdhsa_exception_fp_ieee_inexact 0
		.amdhsa_exception_int_div_zero 0
	.end_amdhsa_kernel

amdhsa.kernels:
  - .agpr_count:     0
    .args:
      - .actual_access:  read_only
        .address_space:  global
        .offset:         0
        .size:           8
        .value_kind:     global_buffer
      - .actual_access:  read_only
        .address_space:  global
        .offset:         8
        .size:           8
        .value_kind:     global_buffer
      - .actual_access:  write_only
        .address_space:  global
        .offset:         16
        .size:           8
        .value_kind:     global_buffer
      - .actual_access:  write_only
        .address_space:  global
        .offset:         24
        .size:           8
        .value_kind:     global_buffer
      - .offset:         32
        .size:           4
        .value_kind:     hidden_block_count_x
      - .offset:         36
        .size:           4
        .value_kind:     hidden_block_count_y
      - .offset:         40
        .size:           4
        .value_kind:     hidden_block_count_z
      - .offset:         44
        .size:           2
        .value_kind:     hidden_group_size_x
      - .offset:         46
        .size:           2
        .value_kind:     hidden_group_size_y
      - .offset:         48
        .size:           2
        .value_kind:     hidden_group_size_z
      - .offset:         50
        .size:           2
        .value_kind:     hidden_remainder_x
      - .offset:         52
        .size:           2
        .value_kind:     hidden_remainder_y
      - .offset:         54
        .size:           2
        .value_kind:     hidden_remainder_z
      - .offset:         72
        .size:           8
        .value_kind:     hidden_global_offset_x
      - .offset:         80
        .size:           8
        .value_kind:     hidden_global_offset_y
      - .offset:         88
        .size:           8
        .value_kind:     hidden_global_offset_z
      - .offset:         96
        .size:           2
        .value_kind:     hidden_grid_dims
    .group_segment_fixed_size: 0
    .kernarg_segment_align: 8
    .kernarg_segment_size: 288
    .language:       OpenCL C
    .language_version:
      - 2
      - 0
    .max_flat_workgroup_size: 256
    .name:           _Z11prep_kernelPKfS0_PfPDv4_DF16_
    .private_segment_fixed_size: 0
    .sgpr_count:     20
    .sgpr_spill_count: 0
    .symbol:         _Z11prep_kernelPKfS0_PfPDv4_DF16_.kd
    .uniform_work_group_size: 1
    .uses_dynamic_stack: false
    .vgpr_count:     17
    .vgpr_spill_count: 0
    .wavefront_size: 64
  - .agpr_count:     0
    .args:
      - .actual_access:  read_only
        .address_space:  global
        .offset:         0
        .size:           8
        .value_kind:     global_buffer
      - .actual_access:  read_only
        .address_space:  global
        .offset:         8
        .size:           8
        .value_kind:     global_buffer
      - .actual_access:  read_only
        .address_space:  global
        .offset:         16
        .size:           8
        .value_kind:     global_buffer
      - .actual_access:  read_only
        .address_space:  global
        .offset:         24
        .size:           8
        .value_kind:     global_buffer
      - .actual_access:  write_only
        .address_space:  global
        .offset:         32
        .size:           8
        .value_kind:     global_buffer
      - .offset:         40
        .size:           4
        .value_kind:     by_value
    .group_segment_fixed_size: 36928
    .kernarg_segment_align: 8
    .kernarg_segment_size: 44
    .language:       OpenCL C
    .language_version:
      - 2
      - 0
    .max_flat_workgroup_size: 512
    .name:           _Z11attn_kernelPKfS0_PKDv8_DF16_S0_Pfi
    .private_segment_fixed_size: 0
    .sgpr_count:     64
    .sgpr_spill_count: 0
    .symbol:         _Z11attn_kernelPKfS0_PKDv8_DF16_S0_Pfi.kd
    .uniform_work_group_size: 1
    .uses_dynamic_stack: false
    .vgpr_count:     248
    .vgpr_spill_count: 0
    .wavefront_size: 64
